# stats2: uniform branch to a 3-slot path for waves whose 8 nodes all have at most 24 neighbours (no masked slot work, no tail loops)
# speedup vs baseline: 1.0015x; 1.0015x over previous
_Z13stats2_kernelPKiS0_PKfS2_S0_P15HIP_vector_typeIfLj4EEi:
	s_load_dwordx8 s[4:11], s[0:1], 0x0
	s_load_dwordx4 s[12:15], s[0:1], 0x20
	s_load_dword s16, s[0:1], 0x30
	v_lshrrev_b32_e32 v1, 3, v0
	v_lshl_or_b32 v1, s2, 5, v1
	v_and_b32_e32 v2, 7, v0
	v_mov_b32_e32 v25, 0xff800000
	s_waitcnt lgkmcnt(0)
	s_add_i32 s17, s16, -1
	v_cmp_gt_i32_e64 s[18:19], s16, v1
	v_min_i32_e32 v1, s17, v1
	v_lshlrev_b32_e32 v3, 2, v1
	global_load_dword v4, v3, s[4:5]
	global_load_dword v5, v3, s[4:5] offset:4
	global_load_dword v6, v3, s[10:11]
	global_load_dword v7, v3, s[8:9]
	global_load_dword v8, v3, s[12:13]
	s_waitcnt vmcnt(3)
	v_sub_u32_e32 v5, v5, v4
	v_add_u32_e32 v9, v4, v2
	v_lshlrev_b32_e32 v9, 2, v9
	v_cmp_lt_i32_e64 s[20:21], v2, v5
	v_add_u32_e32 v23, 8, v2
	v_cmp_lt_i32_e64 s[22:23], v23, v5
	v_add_u32_e32 v23, 16, v2
	v_cmp_lt_i32_e64 s[24:25], v23, v5
	v_add_u32_e32 v23, 24, v2
	v_cmp_lt_i32_e64 s[26:27], v23, v5
	v_add_u32_e32 v23, 32, v2
	v_cmp_lt_i32_e64 s[28:29], v23, v5
	v_add_u32_e32 v23, 40, v2
	v_cmp_lt_i32_e64 s[30:31], v23, v5
	s_cmp_eq_u64 s[26:27], 0
	s_cbranch_scc1 .Lst2_short
	s_mov_b64 exec, s[20:21]
	global_load_dword v10, v9, s[6:7]
	s_mov_b64 exec, s[22:23]
	global_load_dword v11, v9, s[6:7] offset:32
	s_mov_b64 exec, s[24:25]
	global_load_dword v12, v9, s[6:7] offset:64
	s_mov_b64 exec, s[26:27]
	global_load_dword v13, v9, s[6:7] offset:96
	s_mov_b64 exec, s[28:29]
	global_load_dword v14, v9, s[6:7] offset:128
	s_mov_b64 exec, s[30:31]
	global_load_dword v15, v9, s[6:7] offset:160
	s_mov_b64 exec, -1
	s_waitcnt vmcnt(0)
	s_mov_b64 exec, s[20:21]
	v_lshlrev_b32_e32 v10, 2, v10
	global_load_dword v10, v10, s[8:9]
	s_mov_b64 exec, s[22:23]
	v_lshlrev_b32_e32 v11, 2, v11
	global_load_dword v11, v11, s[8:9]
	s_mov_b64 exec, s[24:25]
	v_lshlrev_b32_e32 v12, 2, v12
	global_load_dword v12, v12, s[8:9]
	s_mov_b64 exec, s[26:27]
	v_lshlrev_b32_e32 v13, 2, v13
	global_load_dword v13, v13, s[8:9]
	s_mov_b64 exec, s[28:29]
	v_lshlrev_b32_e32 v14, 2, v14
	global_load_dword v14, v14, s[8:9]
	s_mov_b64 exec, s[30:31]
	v_lshlrev_b32_e32 v15, 2, v15
	global_load_dword v15, v15, s[8:9]
	s_mov_b64 exec, -1
	v_add_f32_e32 v22, v6, v7
	v_mul_f32_e32 v23, 0x3e4ccccd, v22
	v_max_f32_e32 v22, v22, v23
	s_waitcnt vmcnt(0)
	v_add_f32_e32 v16, v6, v10
	v_mul_f32_e32 v23, 0x3e4ccccd, v16
	v_max_f32_e32 v16, v16, v23
	v_cndmask_b32_e64 v16, v25, v16, s[20:21]
	v_add_f32_e32 v17, v6, v11
	v_mul_f32_e32 v23, 0x3e4ccccd, v17
	v_max_f32_e32 v17, v17, v23
	v_cndmask_b32_e64 v17, v25, v17, s[22:23]
	v_add_f32_e32 v18, v6, v12
	v_mul_f32_e32 v23, 0x3e4ccccd, v18
	v_max_f32_e32 v18, v18, v23
	v_cndmask_b32_e64 v18, v25, v18, s[24:25]
	v_add_f32_e32 v19, v6, v13
	v_mul_f32_e32 v23, 0x3e4ccccd, v19
	v_max_f32_e32 v19, v19, v23
	v_cndmask_b32_e64 v19, v25, v19, s[26:27]
	v_add_f32_e32 v20, v6, v14
	v_mul_f32_e32 v23, 0x3e4ccccd, v20
	v_max_f32_e32 v20, v20, v23
	v_cndmask_b32_e64 v20, v25, v20, s[28:29]
	v_add_f32_e32 v21, v6, v15
	v_mul_f32_e32 v23, 0x3e4ccccd, v21
	v_max_f32_e32 v21, v21, v23
	v_cndmask_b32_e64 v21, v25, v21, s[30:31]
	v_max3_f32 v24, v22, v16, v17
	v_max3_f32 v24, v24, v18, v19
	v_max3_f32 v24, v24, v20, v21
	v_add_u32_e32 v26, 48, v2
	v_add_u32_e32 v27, 192, v9

.Lst2_short:
	s_mov_b64 exec, s[20:21]
	global_load_dword v10, v9, s[6:7]
	s_mov_b64 exec, s[22:23]
	global_load_dword v11, v9, s[6:7] offset:32
	s_mov_b64 exec, s[24:25]
	global_load_dword v12, v9, s[6:7] offset:64
	s_mov_b64 exec, -1
	s_waitcnt vmcnt(0)
	s_mov_b64 exec, s[20:21]
	v_lshlrev_b32_e32 v10, 2, v10
	global_load_dword v10, v10, s[8:9]
	s_mov_b64 exec, s[22:23]
	v_lshlrev_b32_e32 v11, 2, v11
	global_load_dword v11, v11, s[8:9]
	s_mov_b64 exec, s[24:25]
	v_lshlrev_b32_e32 v12, 2, v12
	global_load_dword v12, v12, s[8:9]
	s_mov_b64 exec, -1
	v_add_f32_e32 v22, v6, v7
	v_mul_f32_e32 v23, 0x3e4ccccd, v22
	v_max_f32_e32 v22, v22, v23
	s_waitcnt vmcnt(0)
	v_add_f32_e32 v16, v6, v10
	v_mul_f32_e32 v23, 0x3e4ccccd, v16
	v_max_f32_e32 v16, v16, v23
	v_cndmask_b32_e64 v16, v25, v16, s[20:21]
	v_add_f32_e32 v17, v6, v11
	v_mul_f32_e32 v23, 0x3e4ccccd, v17
	v_max_f32_e32 v17, v17, v23
	v_cndmask_b32_e64 v17, v25, v17, s[22:23]
	v_add_f32_e32 v18, v6, v12
	v_mul_f32_e32 v23, 0x3e4ccccd, v18
	v_max_f32_e32 v18, v18, v23
	v_cndmask_b32_e64 v18, v25, v18, s[24:25]
	v_max3_f32 v24, v22, v16, v17
	v_max_f32_e32 v24, v24, v18
	s_nop 1
	v_mov_b32_dpp v23, v24 quad_perm:[1,0,3,2] row_mask:0xf bank_mask:0xf
	v_max_f32_e32 v24, v24, v23
	s_nop 1
	v_mov_b32_dpp v23, v24 quad_perm:[2,3,0,1] row_mask:0xf bank_mask:0xf
	v_max_f32_e32 v24, v24, v23
	s_nop 1
	v_max_f32_dpp v24, v24, v24 row_half_mirror row_mask:0xf bank_mask:0xf
	v_sub_f32_e32 v16, v16, v24
	v_sub_f32_e32 v17, v17, v24
	v_sub_f32_e32 v18, v18, v24
	v_exp_f32_e32 v16, v16
	v_exp_f32_e32 v17, v17
	v_exp_f32_e32 v18, v18
	v_sub_f32_e32 v22, v22, v24
	v_add_f32_e32 v30, v16, v17
	v_add_f32_e32 v30, v30, v18
	s_branch .Lst2_sm_done
